# plus: attention unit prologue issues the rotary-table loads before waiting for the query-fragment loads (one exposed round trip less per unit)
# baseline (speedup 1.0000x reference)
.LBB0_1125:
	s_andn2_b64 vcc, exec, s[0:1]
	v_ashrrev_i32_e32 v201, 31, v200
	s_cbranch_vccnz .LBB0_1127
	v_subrev_u32_e32 v4, s3, v200
	v_add_u32_e32 v4, 0xffffff00, v4
	v_ashrrev_i32_e32 v4, 3, v4
	v_and_b32_e32 v4, -8, v4
	v_lshlrev_b32_e32 v6, 6, v200
	v_ashrrev_i32_e32 v5, 31, v4
	v_and_b32_e32 v6, 0xfc0, v6
	v_mov_b32_e32 v7, v3
	v_lshl_add_u64 v[4:5], v[4:5], 3, v[194:195]
	v_lshl_add_u64 v[20:21], v[196:197], 0, v[6:7]
	global_load_dwordx4 v[12:15], v[4:5], off offset:16
	global_load_dwordx4 v[16:19], v[4:5], off
	s_nop 0
	global_load_dwordx4 v[4:7], v[20:21], off offset:16
	s_nop 0
	global_load_dwordx4 v[20:23], v[20:21], off
	s_waitcnt vmcnt(4)
	v_and_b32_e32 v26, 0xffff0000, v148
	v_lshlrev_b32_e32 v24, 16, v148
	s_waitcnt vmcnt(2)
	v_pk_mul_f32 v[26:27], v[16:17], v[26:27] op_sel:[1,0] op_sel_hi:[0,0]
	v_pk_fma_f32 v[28:29], v[16:17], v[24:25], v[26:27] neg_lo:[0,0,1] neg_hi:[0,0,1]
	v_pk_fma_f32 v[16:17], v[16:17], v[24:25], v[26:27] op_sel_hi:[1,0,1]
	v_and_b32_e32 v24, 0xffff0000, v152
	v_lshlrev_b32_e32 v16, 16, v152
	s_waitcnt vmcnt(0)
	v_pk_mul_f32 v[24:25], v[20:21], v[24:25] op_sel:[1,0] op_sel_hi:[0,0]
	v_cvt_pk_bf16_f32 v148, v28, v17
	v_pk_fma_f32 v[26:27], v[20:21], v[16:17], v[24:25] neg_lo:[0,0,1] neg_hi:[0,0,1]
	v_pk_fma_f32 v[16:17], v[20:21], v[16:17], v[24:25] op_sel_hi:[1,0,1]
	v_and_b32_e32 v20, 0xffff0000, v149
	v_lshlrev_b32_e32 v16, 16, v149
	v_pk_mul_f32 v[20:21], v[18:19], v[20:21] op_sel:[1,0] op_sel_hi:[0,0]
	v_cvt_pk_bf16_f32 v152, v26, v17
	v_pk_fma_f32 v[24:25], v[18:19], v[16:17], v[20:21] neg_lo:[0,0,1] neg_hi:[0,0,1]
	v_pk_fma_f32 v[16:17], v[18:19], v[16:17], v[20:21] op_sel_hi:[1,0,1]
	v_and_b32_e32 v18, 0xffff0000, v153
	v_lshlrev_b32_e32 v16, 16, v153
	v_pk_mul_f32 v[18:19], v[22:23], v[18:19] op_sel:[1,0] op_sel_hi:[0,0]
	v_cvt_pk_bf16_f32 v149, v24, v17
	v_pk_fma_f32 v[20:21], v[22:23], v[16:17], v[18:19] neg_lo:[0,0,1] neg_hi:[0,0,1]
	v_pk_fma_f32 v[16:17], v[22:23], v[16:17], v[18:19] op_sel_hi:[1,0,1]
	v_and_b32_e32 v18, 0xffff0000, v150
	v_lshlrev_b32_e32 v16, 16, v150
	v_pk_mul_f32 v[18:19], v[12:13], v[18:19] op_sel:[1,0] op_sel_hi:[0,0]
	v_cvt_pk_bf16_f32 v153, v20, v17
	v_pk_fma_f32 v[20:21], v[12:13], v[16:17], v[18:19] neg_lo:[0,0,1] neg_hi:[0,0,1]
	v_pk_fma_f32 v[12:13], v[12:13], v[16:17], v[18:19] op_sel_hi:[1,0,1]
	v_and_b32_e32 v16, 0xffff0000, v154
	v_lshlrev_b32_e32 v12, 16, v154
	v_pk_mul_f32 v[16:17], v[4:5], v[16:17] op_sel:[1,0] op_sel_hi:[0,0]
	v_pk_fma_f32 v[18:19], v[4:5], v[12:13], v[16:17] neg_lo:[0,0,1] neg_hi:[0,0,1]
	v_pk_fma_f32 v[4:5], v[4:5], v[12:13], v[16:17] op_sel_hi:[1,0,1]
	v_and_b32_e32 v12, 0xffff0000, v151
	v_cvt_pk_bf16_f32 v150, v20, v13
	v_lshlrev_b32_e32 v4, 16, v151
	v_pk_mul_f32 v[12:13], v[14:15], v[12:13] op_sel:[1,0] op_sel_hi:[0,0]
	v_cvt_pk_bf16_f32 v154, v18, v5
	v_pk_fma_f32 v[16:17], v[14:15], v[4:5], v[12:13] neg_lo:[0,0,1] neg_hi:[0,0,1]
	v_pk_fma_f32 v[4:5], v[14:15], v[4:5], v[12:13] op_sel_hi:[1,0,1]
	v_and_b32_e32 v12, 0xffff0000, v155
	v_lshlrev_b32_e32 v4, 16, v155
	v_pk_mul_f32 v[12:13], v[6:7], v[12:13] op_sel:[1,0] op_sel_hi:[0,0]
	v_cvt_pk_bf16_f32 v151, v16, v5
	v_pk_fma_f32 v[14:15], v[6:7], v[4:5], v[12:13] neg_lo:[0,0,1] neg_hi:[0,0,1]
	v_pk_fma_f32 v[4:5], v[6:7], v[4:5], v[12:13] op_sel_hi:[1,0,1]
	s_nop 0
	v_cvt_pk_bf16_f32 v155, v14, v5
